# first K iteration peeled in P1/P6/P10 GEMM loops (accumulators start from srcC=0, 128 zeroing v_mov per unit removed) on top of V-tile LDS-staged epilogue
# speedup vs baseline: 1.0062x; 1.0062x over previous
; #define PG8_STAGE2(bufoff, gbase, v0, v1) do { \
;         __builtin_amdgcn_global_load_lds((const unsigned*)((const char*)(gbase) + (v0)), (LAS unsigned*)(lds + (bufoff) + ldsw), 16, 0, 0); \
;         __builtin_amdgcn_global_load_lds((const unsigned*)((const char*)(gbase) + (v1)), (LAS unsigned*)(lds + (bufoff) + ldsw + 8192), 16, 0, 0); } while (0)
; #define PG8_STAGE(bufoff, gbase, voff) PG8_STAGE2(bufoff, gbase, (voff)[0], (voff)[1])
; #define PG8_LDA(dst, b, h) do { _Pragma("unroll") for (int m = 0; m < 4; ++m) _Pragma("unroll") for (int k = 0; k < 2; ++k) dst[m][k] = *(const LAS bf16x8*)(lds + PG8_SA(b, h) + aoff + m * 2048 + k * 1024); } while (0)
; #define PG8_BAR __builtin_amdgcn_s_barrier()
; template <class Epi, class Sched, bool ALIGN_EPI, bool SP2, bool GATHER>
; DI void gemm_phase(LAS unsigned char* lds, const Gemm g, const Sched& S, const Epi& E) {
;     ...
;     f32x4 acc[2][2][4][2];
; #pragma unroll
;     for (int a = 0; a < 2; ++a)
; #pragma unroll
;         for (int b = 0; b < 2; ++b)
; #pragma unroll
;             for (int m = 0; m < 4; ++m)
; #pragma unroll
;                 for (int n = 0; n < 2; ++n) acc[a][b][m][n] = (f32x4){0.f, 0.f, 0.f, 0.f};
;     ...
;         for (int t = 0; t < nt; t += 2) {
;             if constexpr (Epi::MID_T >= 0) { if (t == Epi::MID_T) { E.mid(acc, cur, wr, wc, fr, fq); PG8_SCHED; } }
;             const bool last = (t == nt - 2);
;             const char* a1 = cA + (size_t)(t + 1) * kstep;
;             const char* a2 = last ? nA : cA + (size_t)(t + 2) * kstep; const char* b2 = last ? nB : cB + (size_t)(t + 2) * kstep;
;             const char* a3 = a2 + kstep; const char* b3 = b2 + kstep;
;             unsigned x00 = gC[0][0], x01 = gC[0][1], x10 = gC[1][0], x11 = gC[1][1];
;             if constexpr (GATHER) { if (last) { x00 = gN[0][0]; x01 = gN[0][1]; x10 = gN[1][0]; x11 = gN[1][1]; } }
;             PG8_LDB(B0, 0, 0); PG8_LDB(B1, 0, 1); PG8_SCHED; PG8_LDA(At, 0, 0); PG8_STAGE2(PG8_SA(1, 1), a1 + hstepA, gC[1][0], gC[1][1]);
;             PG8_WAIT_V(8); PG8_WAIT_L(0); PG8_BAR; PG8_MMA(0, 0, At, B0); PG8_MMA(0, 1, At, B1); PG8_BAR; PG8_SCHED;
;             PG8_LDA(At, 0, 1); PG8_STAGE(PG8_SB(0, 0), b2, voffB); PG8_STAGE(PG8_SB(0, 1), b2 + hstep, voffB); PG8_STAGE2(PG8_SA(0, 0), a2, x00, x01);
;             PG8_WAIT_V(8); PG8_WAIT_L(0); PG8_BAR; PG8_MMA(1, 0, At, B0); PG8_MMA(1, 1, At, B1); PG8_BAR; PG8_SCHED;
.LBB0_102:
	s_ashr_i32 s51, s50, 31
	s_lshl_b64 s[14:15], s[50:51], 20
	s_add_u32 s52, s3, s14
	s_addc_u32 s53, s63, s15
	s_and_b64 s[14:15], s[8:9], exec
	s_cselect_b32 s5, s53, s11
	s_cselect_b32 s7, s52, s10
	s_ashr_i32 s49, s48, 31
	s_lshl_b64 s[14:15], s[48:49], 20
	s_add_u32 s54, s64, s14
	s_addc_u32 s55, s65, s15
	s_and_b64 s[14:15], s[8:9], exec
	s_cselect_b32 s16, s55, s13
	s_cselect_b32 s17, s54, s12
	s_add_u32 s10, s10, 0x80080
	s_addc_u32 s11, s11, 0
	s_add_u32 s22, s12, 0x100
	s_addc_u32 s38, s13, 0
	s_mov_b32 s39, -2
	ds_read_b128 v[4:7], v175
	ds_read_b128 v[8:11], v175 offset:1024
	ds_read_b128 v[158:161], v175 offset:2048
	ds_read_b128 v[162:165], v175 offset:3072
	ds_read_b128 v[166:169], v176
	ds_read_b128 v[180:183], v176 offset:1024
	ds_read_b128 v[184:187], v176 offset:2048
	ds_read_b128 v[188:191], v176 offset:3072
	s_add_u32 s12, s10, 0xfff80080
	s_addc_u32 s13, s11, -1
	s_cmp_eq_u32 s39, 28
	s_cselect_b32 s15, s5, s13
	s_cselect_b32 s14, s7, s12
	s_cselect_b32 s13, s16, s38
	s_cselect_b32 s12, s17, s22
	s_add_i32 m0, s67, 0xc000
	ds_read_b128 v[192:195], v177
	ds_read_b128 v[196:199], v177 offset:1024
	ds_read_b128 v[200:203], v177 offset:2048
	ds_read_b128 v[204:207], v177 offset:3072
	ds_read_b128 v[208:211], v177 offset:4096
	ds_read_b128 v[212:215], v177 offset:5120
	ds_read_b128 v[216:219], v177 offset:6144
	ds_read_b128 v[220:223], v177 offset:7168
	global_load_lds_dwordx4 v150, s[10:11]
	s_add_i32 m0, s67, 0xe000
	s_nop 0
	global_load_lds_dwordx4 v152, s[10:11]
	s_waitcnt vmcnt(8)
	s_waitcnt lgkmcnt(0)
	s_barrier
	s_setprio 1
	s_waitcnt lgkmcnt(0)
	v_mfma_f32_16x16x32_bf16 v[136:139], v[4:7], v[192:195], 0
	v_mfma_f32_16x16x32_bf16 v[132:135], v[158:161], v[192:195], 0
	v_mfma_f32_16x16x32_bf16 v[128:131], v[4:7], v[200:203], 0
	v_mfma_f32_16x16x32_bf16 v[124:127], v[158:161], v[200:203], 0
	v_mfma_f32_16x16x32_bf16 v[120:123], v[4:7], v[208:211], 0
	v_mfma_f32_16x16x32_bf16 v[116:119], v[158:161], v[208:211], 0
	v_mfma_f32_16x16x32_bf16 v[112:115], v[4:7], v[216:219], 0
	v_mfma_f32_16x16x32_bf16 v[108:111], v[158:161], v[216:219], 0
	v_mfma_f32_16x16x32_bf16 v[136:139], v[8:11], v[196:199], v[136:139]
	v_mfma_f32_16x16x32_bf16 v[132:135], v[162:165], v[196:199], v[132:135]
	v_mfma_f32_16x16x32_bf16 v[128:131], v[8:11], v[204:207], v[128:131]
	v_mfma_f32_16x16x32_bf16 v[124:127], v[162:165], v[204:207], v[124:127]
	v_mfma_f32_16x16x32_bf16 v[120:123], v[8:11], v[212:215], v[120:123]
	v_mfma_f32_16x16x32_bf16 v[116:119], v[162:165], v[212:215], v[116:119]
	v_mfma_f32_16x16x32_bf16 v[112:115], v[8:11], v[220:223], v[112:115]
	v_mfma_f32_16x16x32_bf16 v[108:111], v[162:165], v[220:223], v[108:111]
	s_setprio 0
	s_setprio 1
	v_mfma_f32_16x16x32_bf16 v[72:75], v[166:169], v[192:195], 0
	v_mfma_f32_16x16x32_bf16 v[68:71], v[184:187], v[192:195], 0
	v_mfma_f32_16x16x32_bf16 v[64:67], v[166:169], v[200:203], 0
	v_mfma_f32_16x16x32_bf16 v[60:63], v[184:187], v[200:203], 0
	v_mfma_f32_16x16x32_bf16 v[56:59], v[166:169], v[208:211], 0
	v_mfma_f32_16x16x32_bf16 v[52:55], v[184:187], v[208:211], 0
	v_mfma_f32_16x16x32_bf16 v[48:51], v[166:169], v[216:219], 0
	v_mfma_f32_16x16x32_bf16 v[44:47], v[184:187], v[216:219], 0
	v_mfma_f32_16x16x32_bf16 v[72:75], v[180:183], v[196:199], v[72:75]
	v_mfma_f32_16x16x32_bf16 v[68:71], v[188:191], v[196:199], v[68:71]
	v_mfma_f32_16x16x32_bf16 v[64:67], v[180:183], v[204:207], v[64:67]
	v_mfma_f32_16x16x32_bf16 v[60:63], v[188:191], v[204:207], v[60:63]
	v_mfma_f32_16x16x32_bf16 v[56:59], v[180:183], v[212:215], v[56:59]
	v_mfma_f32_16x16x32_bf16 v[52:55], v[188:191], v[212:215], v[52:55]
	v_mfma_f32_16x16x32_bf16 v[48:51], v[180:183], v[220:223], v[48:51]
	v_mfma_f32_16x16x32_bf16 v[44:47], v[188:191], v[220:223], v[44:47]
	s_setprio 0
	s_barrier
	s_add_i32 s49, s78, s66
	s_add_u32 s98, s12, 0x80
	s_addc_u32 s99, s13, 0
	s_mov_b32 m0, s49
	ds_read_b128 v[192:195], v177 offset:16384
	ds_read_b128 v[196:199], v177 offset:17408
	ds_read_b128 v[200:203], v177 offset:18432
	ds_read_b128 v[204:207], v177 offset:19456
	ds_read_b128 v[208:211], v177 offset:20480
	ds_read_b128 v[212:215], v177 offset:21504
	ds_read_b128 v[216:219], v177 offset:22528
	ds_read_b128 v[220:223], v177 offset:23552
	global_load_lds_dwordx4 v142, s[12:13]
	s_add_i32 m0, s49, 0x2000
	s_add_u32 s56, s12, 0x80000
	s_addc_u32 s57, s13, 0
	s_add_i32 s49, s79, s66
	global_load_lds_dwordx4 v146, s[12:13]
	s_mov_b32 m0, s49
	s_add_u32 s100, s14, 0x80
	s_addc_u32 s101, s15, 0
	global_load_lds_dwordx4 v142, s[56:57]
	s_add_i32 m0, s49, 0x2000
	s_nop 0
	global_load_lds_dwordx4 v146, s[56:57]
	s_mov_b32 m0, s67
	s_nop 0
	global_load_lds_dwordx4 v140, s[14:15]
	s_mov_b32 m0, s68
	s_nop 0
	global_load_lds_dwordx4 v144, s[14:15]
	s_waitcnt vmcnt(8)
	s_waitcnt lgkmcnt(0)
	s_barrier
; #define PG8_STAGE2(bufoff, gbase, v0, v1) do { \
;         __builtin_amdgcn_global_load_lds((const unsigned*)((const char*)(gbase) + (v0)), (LAS unsigned*)(lds + (bufoff) + ldsw), 16, 0, 0); \
;         __builtin_amdgcn_global_load_lds((const unsigned*)((const char*)(gbase) + (v1)), (LAS unsigned*)(lds + (bufoff) + ldsw + 8192), 16, 0, 0); } while (0)
; #define PG8_STAGE(bufoff, gbase, voff) PG8_STAGE2(bufoff, gbase, (voff)[0], (voff)[1])
; #define PG8_LDA(dst, b, h) do { _Pragma("unroll") for (int m = 0; m < 4; ++m) _Pragma("unroll") for (int k = 0; k < 2; ++k) dst[m][k] = *(const LAS bf16x8*)(lds + PG8_SA(b, h) + aoff + m * 2048 + k * 1024); } while (0)
; #define PG8_LDB(dst, b, h) do { _Pragma("unroll") for (int n = 0; n < 2; ++n) _Pragma("unroll") for (int k = 0; k < 2; ++k) dst[n][k] = *(const LAS bf16x8*)(lds + PG8_SB(b, h) + boff + n * 2048 + k * 1024); } while (0)
; #define PG8_MMA(ai, bj, At, Bt) do { __builtin_amdgcn_s_setprio(1); _Pragma("unroll") for (int m = 0; m < 4; ++m) _Pragma("unroll") for (int n = 0; n < 2; ++n) _Pragma("unroll") for (int k = 0; k < 2; ++k) \
;         acc[ai][bj][m][n] = __builtin_amdgcn_mfma_f32_16x16x32_bf16(Bt[n][k], At[m][k], acc[ai][bj][m][n], 0, 0, 0); __builtin_amdgcn_s_setprio(0); } while (0)
; #define PG8_WAIT_V(n) asm volatile("s_waitcnt vmcnt(" #n ")" ::: "memory")
; #define PG8_WAIT_L(n) asm volatile("s_waitcnt lgkmcnt(" #n ")" ::: "memory")
; #define PG8_BAR __builtin_amdgcn_s_barrier()
; #define PG8_SCHED __builtin_amdgcn_sched_barrier(0)
; template <class Epi, class Sched, bool ALIGN_EPI, bool SP2, bool GATHER>
; DI void gemm_phase(LAS unsigned char* lds, const Gemm g, const Sched& S, const Epi& E) {
;     ...
;             PG8_WAIT_V(8); PG8_WAIT_L(0); PG8_BAR; PG8_MMA(0, 0, At, B0); PG8_MMA(0, 1, At, B1); PG8_BAR; PG8_SCHED;
;             PG8_LDA(At, 0, 1); PG8_STAGE(PG8_SB(0, 0), b2, voffB); PG8_STAGE(PG8_SB(0, 1), b2 + hstep, voffB); PG8_STAGE2(PG8_SA(0, 0), a2, x00, x01);
;             PG8_WAIT_V(8); PG8_WAIT_L(0); PG8_BAR; PG8_MMA(1, 0, At, B0); PG8_MMA(1, 1, At, B1); PG8_BAR; PG8_SCHED;
;             PG8_LDB(B0, 1, 0); PG8_LDB(B1, 1, 1); PG8_SCHED; PG8_LDA(At, 1, 0); PG8_STAGE2(PG8_SA(0, 1), a2 + hstepA, x10, x11);
;             PG8_WAIT_V(8); PG8_WAIT_L(0); PG8_BAR; PG8_MMA(0, 0, At, B0); PG8_MMA(0, 1, At, B1); PG8_BAR; PG8_SCHED;
	s_setprio 1
	s_waitcnt lgkmcnt(0)
	v_mfma_f32_16x16x32_bf16 v[104:107], v[4:7], v[192:195], 0
	v_mfma_f32_16x16x32_bf16 v[100:103], v[158:161], v[192:195], 0
	v_mfma_f32_16x16x32_bf16 v[96:99], v[4:7], v[200:203], 0
	v_mfma_f32_16x16x32_bf16 v[92:95], v[158:161], v[200:203], 0
	v_mfma_f32_16x16x32_bf16 v[88:91], v[4:7], v[208:211], 0
	v_mfma_f32_16x16x32_bf16 v[84:87], v[158:161], v[208:211], 0
	v_mfma_f32_16x16x32_bf16 v[4:7], v[4:7], v[216:219], 0
	v_mfma_f32_16x16x32_bf16 v[104:107], v[8:11], v[196:199], v[104:107]
	v_mfma_f32_16x16x32_bf16 v[100:103], v[162:165], v[196:199], v[100:103]
	v_mfma_f32_16x16x32_bf16 v[96:99], v[8:11], v[204:207], v[96:99]
	v_mfma_f32_16x16x32_bf16 v[92:95], v[162:165], v[204:207], v[92:95]
	v_mfma_f32_16x16x32_bf16 v[88:91], v[8:11], v[212:215], v[88:91]
	v_mfma_f32_16x16x32_bf16 v[84:87], v[162:165], v[212:215], v[84:87]
	v_mfma_f32_16x16x32_bf16 v[4:7], v[8:11], v[220:223], v[4:7]
	v_mfma_f32_16x16x32_bf16 v[8:11], v[158:161], v[216:219], 0
	v_mfma_f32_16x16x32_bf16 v[8:11], v[162:165], v[220:223], v[8:11]
	s_setprio 0
	s_setprio 1
	v_mfma_f32_16x16x32_bf16 v[40:43], v[166:169], v[192:195], 0
	v_mfma_f32_16x16x32_bf16 v[36:39], v[184:187], v[192:195], 0
	v_mfma_f32_16x16x32_bf16 v[32:35], v[166:169], v[200:203], 0
	v_mfma_f32_16x16x32_bf16 v[28:31], v[184:187], v[200:203], 0
	v_mfma_f32_16x16x32_bf16 v[24:27], v[166:169], v[208:211], 0
	v_mfma_f32_16x16x32_bf16 v[20:23], v[184:187], v[208:211], 0
	v_mfma_f32_16x16x32_bf16 v[16:19], v[166:169], v[216:219], 0
	v_mfma_f32_16x16x32_bf16 v[12:15], v[184:187], v[216:219], 0
	v_mfma_f32_16x16x32_bf16 v[40:43], v[180:183], v[196:199], v[40:43]
	v_mfma_f32_16x16x32_bf16 v[36:39], v[188:191], v[196:199], v[36:39]
	v_mfma_f32_16x16x32_bf16 v[32:35], v[180:183], v[204:207], v[32:35]
	v_mfma_f32_16x16x32_bf16 v[28:31], v[188:191], v[204:207], v[28:31]
	v_mfma_f32_16x16x32_bf16 v[24:27], v[180:183], v[212:215], v[24:27]
	v_mfma_f32_16x16x32_bf16 v[20:23], v[188:191], v[212:215], v[20:23]
	v_mfma_f32_16x16x32_bf16 v[16:19], v[180:183], v[220:223], v[16:19]
	v_mfma_f32_16x16x32_bf16 v[12:15], v[188:191], v[220:223], v[12:15]
	s_setprio 0
	s_barrier
	s_add_i32 s49, 0, 0x18000
	v_add_u32_e32 v3, s49, v172
	s_add_i32 s51, 0, 0x1c000
	ds_read_b128 v[76:79], v3
	ds_read_b128 v[80:83], v3 offset:1024
	ds_read_b128 v[158:161], v3 offset:2048
	ds_read_b128 v[162:165], v3 offset:3072
	v_add_u32_e32 v3, s51, v172
	ds_read_b128 v[166:169], v3
	ds_read_b128 v[180:183], v3 offset:1024
	ds_read_b128 v[184:187], v3 offset:2048
	ds_read_b128 v[188:191], v3 offset:3072
	s_add_u32 s14, s14, 0x80000
	s_addc_u32 s15, s15, 0
	s_mov_b32 m0, s69
	ds_read_b128 v[192:195], v177 offset:32768
	ds_read_b128 v[196:199], v177 offset:33792
	ds_read_b128 v[200:203], v177 offset:34816
	ds_read_b128 v[204:207], v177 offset:35840
	ds_read_b128 v[208:211], v177 offset:36864
	ds_read_b128 v[212:215], v177 offset:37888
	ds_read_b128 v[216:219], v177 offset:38912
	ds_read_b128 v[220:223], v177 offset:39936
	global_load_lds_dwordx4 v140, s[14:15]
	s_mov_b32 m0, s70
	s_nop 0
	global_load_lds_dwordx4 v144, s[14:15]
	s_waitcnt vmcnt(8)
	s_waitcnt lgkmcnt(0)
	s_barrier
	s_setprio 1
	s_waitcnt lgkmcnt(0)
	v_mfma_f32_16x16x32_bf16 v[136:139], v[76:79], v[192:195], v[136:139]
	v_mfma_f32_16x16x32_bf16 v[132:135], v[158:161], v[192:195], v[132:135]
	v_mfma_f32_16x16x32_bf16 v[128:131], v[76:79], v[200:203], v[128:131]
	v_mfma_f32_16x16x32_bf16 v[124:127], v[158:161], v[200:203], v[124:127]
	v_mfma_f32_16x16x32_bf16 v[120:123], v[76:79], v[208:211], v[120:123]
	v_mfma_f32_16x16x32_bf16 v[116:119], v[158:161], v[208:211], v[116:119]
	v_mfma_f32_16x16x32_bf16 v[112:115], v[76:79], v[216:219], v[112:115]
	v_mfma_f32_16x16x32_bf16 v[108:111], v[158:161], v[216:219], v[108:111]
	v_mfma_f32_16x16x32_bf16 v[136:139], v[80:83], v[196:199], v[136:139]
	v_mfma_f32_16x16x32_bf16 v[132:135], v[162:165], v[196:199], v[132:135]
	v_mfma_f32_16x16x32_bf16 v[128:131], v[80:83], v[204:207], v[128:131]
	v_mfma_f32_16x16x32_bf16 v[124:127], v[162:165], v[204:207], v[124:127]
	v_mfma_f32_16x16x32_bf16 v[120:123], v[80:83], v[212:215], v[120:123]
	v_mfma_f32_16x16x32_bf16 v[116:119], v[162:165], v[212:215], v[116:119]
	v_mfma_f32_16x16x32_bf16 v[112:115], v[80:83], v[220:223], v[112:115]
	v_mfma_f32_16x16x32_bf16 v[108:111], v[162:165], v[220:223], v[108:111]
	s_setprio 0
	s_setprio 1
	v_mfma_f32_16x16x32_bf16 v[72:75], v[166:169], v[192:195], v[72:75]
	v_mfma_f32_16x16x32_bf16 v[68:71], v[184:187], v[192:195], v[68:71]
	v_mfma_f32_16x16x32_bf16 v[64:67], v[166:169], v[200:203], v[64:67]
	v_mfma_f32_16x16x32_bf16 v[60:63], v[184:187], v[200:203], v[60:63]
	v_mfma_f32_16x16x32_bf16 v[56:59], v[166:169], v[208:211], v[56:59]
	v_mfma_f32_16x16x32_bf16 v[52:55], v[184:187], v[208:211], v[52:55]
	v_mfma_f32_16x16x32_bf16 v[48:51], v[166:169], v[216:219], v[48:51]
	v_mfma_f32_16x16x32_bf16 v[44:47], v[184:187], v[216:219], v[44:47]
	v_mfma_f32_16x16x32_bf16 v[72:75], v[180:183], v[196:199], v[72:75]
	v_mfma_f32_16x16x32_bf16 v[68:71], v[188:191], v[196:199], v[68:71]
	v_mfma_f32_16x16x32_bf16 v[64:67], v[180:183], v[204:207], v[64:67]
	v_mfma_f32_16x16x32_bf16 v[60:63], v[188:191], v[204:207], v[60:63]
	v_mfma_f32_16x16x32_bf16 v[56:59], v[180:183], v[212:215], v[56:59]
	v_mfma_f32_16x16x32_bf16 v[52:55], v[188:191], v[212:215], v[52:55]
	v_mfma_f32_16x16x32_bf16 v[48:51], v[180:183], v[220:223], v[48:51]
	v_mfma_f32_16x16x32_bf16 v[44:47], v[188:191], v[220:223], v[44:47]
	s_setprio 0
	s_barrier
; #define PG8_STAGE2(bufoff, gbase, v0, v1) do { \
;         __builtin_amdgcn_global_load_lds((const unsigned*)((const char*)(gbase) + (v0)), (LAS unsigned*)(lds + (bufoff) + ldsw), 16, 0, 0); \
;         __builtin_amdgcn_global_load_lds((const unsigned*)((const char*)(gbase) + (v1)), (LAS unsigned*)(lds + (bufoff) + ldsw + 8192), 16, 0, 0); } while (0)
; #define PG8_STAGE(bufoff, gbase, voff) PG8_STAGE2(bufoff, gbase, (voff)[0], (voff)[1])
; #define PG8_LDA(dst, b, h) do { _Pragma("unroll") for (int m = 0; m < 4; ++m) _Pragma("unroll") for (int k = 0; k < 2; ++k) dst[m][k] = *(const LAS bf16x8*)(lds + PG8_SA(b, h) + aoff + m * 2048 + k * 1024); } while (0)
; #define PG8_LDB(dst, b, h) do { _Pragma("unroll") for (int n = 0; n < 2; ++n) _Pragma("unroll") for (int k = 0; k < 2; ++k) dst[n][k] = *(const LAS bf16x8*)(lds + PG8_SB(b, h) + boff + n * 2048 + k * 1024); } while (0)
; #define PG8_MMA(ai, bj, At, Bt) do { __builtin_amdgcn_s_setprio(1); _Pragma("unroll") for (int m = 0; m < 4; ++m) _Pragma("unroll") for (int n = 0; n < 2; ++n) _Pragma("unroll") for (int k = 0; k < 2; ++k) \
;         acc[ai][bj][m][n] = __builtin_amdgcn_mfma_f32_16x16x32_bf16(Bt[n][k], At[m][k], acc[ai][bj][m][n], 0, 0, 0); __builtin_amdgcn_s_setprio(0); } while (0)
; #define PG8_WAIT_V(n) asm volatile("s_waitcnt vmcnt(" #n ")" ::: "memory")
; #define PG8_WAIT_L(n) asm volatile("s_waitcnt lgkmcnt(" #n ")" ::: "memory")
; #define PG8_BAR __builtin_amdgcn_s_barrier()
; #define PG8_SCHED __builtin_amdgcn_sched_barrier(0)
; template <class Epi, class Sched, bool ALIGN_EPI, bool SP2, bool GATHER>
; DI void gemm_phase(LAS unsigned char* lds, const Gemm g, const Sched& S, const Epi& E) {
;     ...
;             PG8_LDB(B0, 1, 0); PG8_LDB(B1, 1, 1); PG8_SCHED; PG8_LDA(At, 1, 0); PG8_STAGE2(PG8_SA(0, 1), a2 + hstepA, x10, x11);
;             PG8_WAIT_V(8); PG8_WAIT_L(0); PG8_BAR; PG8_MMA(0, 0, At, B0); PG8_MMA(0, 1, At, B1); PG8_BAR; PG8_SCHED;
;             PG8_LDA(At, 1, 1); PG8_STAGE(PG8_SB(1, 0), b3, voffB); PG8_STAGE(PG8_SB(1, 1), b3 + hstep, voffB); PG8_STAGE2(PG8_SA(1, 0), a3, x00, x01);
;             PG8_WAIT_V(8); PG8_WAIT_L(0); PG8_BAR; PG8_MMA(1, 0, At, B0); PG8_MMA(1, 1, At, B1); PG8_BAR; PG8_SCHED;
;         }
	s_add_i32 s14, s49, s66
	s_mov_b32 m0, s14
	ds_read_b128 v[192:195], v177 offset:49152
	ds_read_b128 v[196:199], v177 offset:50176
	ds_read_b128 v[200:203], v177 offset:51200
	ds_read_b128 v[204:207], v177 offset:52224
	ds_read_b128 v[208:211], v177 offset:53248
	ds_read_b128 v[212:215], v177 offset:54272
	ds_read_b128 v[216:219], v177 offset:55296
	ds_read_b128 v[220:223], v177 offset:56320
	global_load_lds_dwordx4 v142, s[98:99]
	s_add_i32 m0, s14, 0x2000
	s_add_u32 s12, s12, 0x80080
	s_addc_u32 s13, s13, 0
	s_add_i32 s14, s51, s66
	global_load_lds_dwordx4 v146, s[98:99]
	s_mov_b32 m0, s14
	s_nop 0
	global_load_lds_dwordx4 v142, s[12:13]
	s_add_i32 m0, s14, 0x2000
	s_nop 0
	global_load_lds_dwordx4 v146, s[12:13]
	s_mov_b32 m0, s73
	s_nop 0
	global_load_lds_dwordx4 v140, s[100:101]
	s_mov_b32 m0, s74
	s_nop 0
	global_load_lds_dwordx4 v144, s[100:101]
	s_waitcnt vmcnt(8)
	s_waitcnt lgkmcnt(0)
	s_barrier
	s_setprio 1
	s_waitcnt lgkmcnt(0)
	v_mfma_f32_16x16x32_bf16 v[104:107], v[76:79], v[192:195], v[104:107]
	v_mfma_f32_16x16x32_bf16 v[96:99], v[76:79], v[200:203], v[96:99]
	v_mfma_f32_16x16x32_bf16 v[88:91], v[76:79], v[208:211], v[88:91]
	v_mfma_f32_16x16x32_bf16 v[4:7], v[76:79], v[216:219], v[4:7]
	v_mfma_f32_16x16x32_bf16 v[104:107], v[80:83], v[196:199], v[104:107]
	v_mfma_f32_16x16x32_bf16 v[100:103], v[158:161], v[192:195], v[100:103]
	v_mfma_f32_16x16x32_bf16 v[96:99], v[80:83], v[204:207], v[96:99]
	v_mfma_f32_16x16x32_bf16 v[92:95], v[158:161], v[200:203], v[92:95]
	v_mfma_f32_16x16x32_bf16 v[88:91], v[80:83], v[212:215], v[88:91]
	v_mfma_f32_16x16x32_bf16 v[84:87], v[158:161], v[208:211], v[84:87]
	v_mfma_f32_16x16x32_bf16 v[80:83], v[80:83], v[220:223], v[4:7]
	v_mfma_f32_16x16x32_bf16 v[4:7], v[158:161], v[216:219], v[8:11]
	v_mfma_f32_16x16x32_bf16 v[100:103], v[162:165], v[196:199], v[100:103]
	v_mfma_f32_16x16x32_bf16 v[92:95], v[162:165], v[204:207], v[92:95]
	v_mfma_f32_16x16x32_bf16 v[84:87], v[162:165], v[212:215], v[84:87]
	v_mfma_f32_16x16x32_bf16 v[76:79], v[162:165], v[220:223], v[4:7]
	s_setprio 0
	s_setprio 1
	v_mfma_f32_16x16x32_bf16 v[4:7], v[166:169], v[192:195], v[40:43]
	v_mfma_f32_16x16x32_bf16 v[40:43], v[180:183], v[196:199], v[4:7]
	v_mfma_f32_16x16x32_bf16 v[4:7], v[184:187], v[192:195], v[36:39]
	v_mfma_f32_16x16x32_bf16 v[36:39], v[188:191], v[196:199], v[4:7]
	v_mfma_f32_16x16x32_bf16 v[4:7], v[166:169], v[200:203], v[32:35]
	v_mfma_f32_16x16x32_bf16 v[32:35], v[180:183], v[204:207], v[4:7]
	v_mfma_f32_16x16x32_bf16 v[4:7], v[184:187], v[200:203], v[28:31]
	v_mfma_f32_16x16x32_bf16 v[28:31], v[188:191], v[204:207], v[4:7]
	v_mfma_f32_16x16x32_bf16 v[4:7], v[166:169], v[208:211], v[24:27]
	v_mfma_f32_16x16x32_bf16 v[24:27], v[180:183], v[212:215], v[4:7]
	v_mfma_f32_16x16x32_bf16 v[4:7], v[184:187], v[208:211], v[20:23]
	v_mfma_f32_16x16x32_bf16 v[20:23], v[188:191], v[212:215], v[4:7]
	v_mfma_f32_16x16x32_bf16 v[4:7], v[166:169], v[216:219], v[16:19]
	v_mfma_f32_16x16x32_bf16 v[16:19], v[180:183], v[220:223], v[4:7]
	v_mfma_f32_16x16x32_bf16 v[4:7], v[184:187], v[216:219], v[12:15]
	v_mfma_f32_16x16x32_bf16 v[12:15], v[188:191], v[220:223], v[4:7]
	s_setprio 0
	s_barrier
	s_add_i32 s39, s39, 2
	s_add_u32 s10, s10, 0x100
	s_addc_u32 s11, s11, 0
	s_add_u32 s22, s22, 0x100
	s_addc_u32 s38, s38, 0
	s_cmp_gt_u32 s39, 29
	s_cbranch_scc1 .Lpeel_exit_p1

; #define PG8_BAR __builtin_amdgcn_s_barrier()
; template <class Epi, class Sched, bool ALIGN_EPI, bool SP2, bool GATHER>
; DI void gemm_phase(LAS unsigned char* lds, const Gemm g, const Sched& S, const Epi& E) {
;     ...
;         if constexpr (ALIGN_EPI) { if (wr == 0) PG8_BAR; }
;         E(acc, cur, wr, wc, fr, fq);
.Lpeel_exit_p1:
	s_and_b64 vcc, exec, s[30:31]
	s_cbranch_vccz .LBB0_106
	s_barrier

; #define PG8_STAGE2(bufoff, gbase, v0, v1) do { \
;         __builtin_amdgcn_global_load_lds((const unsigned*)((const char*)(gbase) + (v0)), (LAS unsigned*)(lds + (bufoff) + ldsw), 16, 0, 0); \
;         __builtin_amdgcn_global_load_lds((const unsigned*)((const char*)(gbase) + (v1)), (LAS unsigned*)(lds + (bufoff) + ldsw + 8192), 16, 0, 0); } while (0)
; #define PG8_STAGE(bufoff, gbase, voff) PG8_STAGE2(bufoff, gbase, (voff)[0], (voff)[1])
; #define PG8_LDA(dst, b, h) do { _Pragma("unroll") for (int m = 0; m < 4; ++m) _Pragma("unroll") for (int k = 0; k < 2; ++k) dst[m][k] = *(const LAS bf16x8*)(lds + PG8_SA(b, h) + aoff + m * 2048 + k * 1024); } while (0)
; #define PG8_WAIT_V(n) asm volatile("s_waitcnt vmcnt(" #n ")" ::: "memory")
; template <class Epi, class Sched, bool ALIGN_EPI, bool SP2, bool GATHER>
; DI void gemm_phase(LAS unsigned char* lds, const Gemm g, const Sched& S, const Epi& E) {
;     ...
;             const bool last = (t == nt - 2);
;             const char* a1 = cA + (size_t)(t + 1) * kstep;
;             const char* a2 = last ? nA : cA + (size_t)(t + 2) * kstep; const char* b2 = last ? nB : cB + (size_t)(t + 2) * kstep;
;             const char* a3 = a2 + kstep; const char* b3 = b2 + kstep;
;             unsigned x00 = gC[0][0], x01 = gC[0][1], x10 = gC[1][0], x11 = gC[1][1];
;             if constexpr (GATHER) { if (last) { x00 = gN[0][0]; x01 = gN[0][1]; x10 = gN[1][0]; x11 = gN[1][1]; } }
;             PG8_LDB(B0, 0, 0); PG8_LDB(B1, 0, 1); PG8_SCHED; PG8_LDA(At, 0, 0); PG8_STAGE2(PG8_SA(1, 1), a1 + hstepA, gC[1][0], gC[1][1]);
;             PG8_WAIT_V(8); PG8_WAIT_L(0); PG8_BAR; PG8_MMA(0, 0, At, B0); PG8_MMA(0, 1, At, B1); PG8_BAR; PG8_SCHED;
;             PG8_LDA(At, 0, 1); PG8_STAGE(PG8_SB(0, 0), b2, voffB); PG8_STAGE(PG8_SB(0, 1), b2 + hstep, voffB); PG8_STAGE2(PG8_SA(0, 0), a2, x00, x01);
;             PG8_WAIT_V(8); PG8_WAIT_L(0); PG8_BAR; PG8_MMA(1, 0, At, B0); PG8_MMA(1, 1, At, B1); PG8_BAR; PG8_SCHED;
;             PG8_LDB(B0, 1, 0); PG8_LDB(B1, 1, 1); PG8_SCHED; PG8_LDA(At, 1, 0); PG8_STAGE2(PG8_SA(0, 1), a2 + hstepA, x10, x11);
;             PG8_WAIT_V(8); PG8_WAIT_L(0); PG8_BAR; PG8_MMA(0, 0, At, B0); PG8_MMA(0, 1, At, B1); PG8_BAR; PG8_SCHED;
;     ...
;                 for (int m = 0; m < 4; ++m)
; #pragma unroll
;                     for (int n = 0; n < 2; ++n) acc[a][b][m][n] = (f32x4){0.f, 0.f, 0.f, 0.f};
.LBB0_673:
	s_ashr_i32 s27, s26, 31
	s_lshl_b64 s[28:29], s[26:27], 20
	s_add_u32 s28, s38, s28
	s_addc_u32 s29, s39, s29
	s_and_b64 s[30:31], s[4:5], exec
	s_cselect_b32 s27, s29, s37
	s_cselect_b32 s57, s28, s36
	s_ashr_i32 s25, s24, 31
	s_lshl_b64 s[30:31], s[24:25], 20
	s_add_u32 s30, s44, s30
	s_addc_u32 s31, s45, s31
	s_and_b64 s[42:43], s[4:5], exec
	s_cselect_b32 s25, s31, s41
	s_cselect_b32 s63, s30, s40
	s_add_u32 s36, s36, 0x80080
	s_addc_u32 s37, s37, 0
	s_add_u32 s64, s40, 0x100
	s_addc_u32 s65, s41, 0
	s_mov_b32 s66, -2
	ds_read_b128 v[146:149], v154
	ds_read_b128 v[158:161], v154 offset:1024
	ds_read_b128 v[162:165], v154 offset:2048
	ds_read_b128 v[166:169], v154 offset:3072
	ds_read_b128 v[170:173], v155
	ds_read_b128 v[174:177], v155 offset:1024
	ds_read_b128 v[178:181], v155 offset:2048
	ds_read_b128 v[182:185], v155 offset:3072
	s_add_u32 s40, s36, 0xfff80080
	s_addc_u32 s41, s37, -1
	s_cmp_eq_u32 s66, 28
	s_cselect_b32 s43, s27, s41
	s_cselect_b32 s42, s57, s40
	s_cselect_b32 s41, s25, s65
	s_cselect_b32 s40, s63, s64
	v_lshl_add_u64 v[150:151], s[36:37], 0, v[138:139]
	s_add_i32 m0, s35, 0xc000
	ds_read_b128 v[186:189], v156
	ds_read_b128 v[190:193], v156 offset:1024
	ds_read_b128 v[194:197], v156 offset:2048
	ds_read_b128 v[198:201], v156 offset:3072
	ds_read_b128 v[202:205], v156 offset:4096
	ds_read_b128 v[206:209], v156 offset:5120
	ds_read_b128 v[210:213], v156 offset:6144
	ds_read_b128 v[214:217], v156 offset:7168
	global_load_lds_dwordx4 v[150:151], off
	v_lshl_add_u64 v[150:151], s[36:37], 0, v[140:141]
	s_add_i32 m0, s35, 0xe000
	s_nop 0
	global_load_lds_dwordx4 v[150:151], off
	s_waitcnt vmcnt(8)
	s_waitcnt lgkmcnt(0)
	s_barrier
	s_setprio 1
	s_waitcnt lgkmcnt(0)
	v_mfma_f32_16x16x32_bf16 v[126:129], v[146:149], v[186:189], 0
	v_mfma_f32_16x16x32_bf16 v[122:125], v[162:165], v[186:189], 0
	v_mfma_f32_16x16x32_bf16 v[110:113], v[146:149], v[194:197], 0
	v_mfma_f32_16x16x32_bf16 v[106:109], v[162:165], v[194:197], 0
	v_mfma_f32_16x16x32_bf16 v[94:97], v[146:149], v[202:205], 0
	v_mfma_f32_16x16x32_bf16 v[90:93], v[162:165], v[202:205], 0
	v_mfma_f32_16x16x32_bf16 v[78:81], v[146:149], v[210:213], 0
	v_mfma_f32_16x16x32_bf16 v[74:77], v[162:165], v[210:213], 0
	v_mfma_f32_16x16x32_bf16 v[126:129], v[158:161], v[190:193], v[126:129]
	v_mfma_f32_16x16x32_bf16 v[122:125], v[166:169], v[190:193], v[122:125]
	v_mfma_f32_16x16x32_bf16 v[110:113], v[158:161], v[198:201], v[110:113]
	v_mfma_f32_16x16x32_bf16 v[106:109], v[166:169], v[198:201], v[106:109]
	v_mfma_f32_16x16x32_bf16 v[94:97], v[158:161], v[206:209], v[94:97]
	v_mfma_f32_16x16x32_bf16 v[90:93], v[166:169], v[206:209], v[90:93]
	v_mfma_f32_16x16x32_bf16 v[78:81], v[158:161], v[214:217], v[78:81]
	v_mfma_f32_16x16x32_bf16 v[74:77], v[166:169], v[214:217], v[74:77]
	s_setprio 0
	s_setprio 1
	v_mfma_f32_16x16x32_bf16 v[118:121], v[170:173], v[186:189], 0
	v_mfma_f32_16x16x32_bf16 v[114:117], v[178:181], v[186:189], 0
	v_mfma_f32_16x16x32_bf16 v[102:105], v[170:173], v[194:197], 0
	v_mfma_f32_16x16x32_bf16 v[98:101], v[178:181], v[194:197], 0
	v_mfma_f32_16x16x32_bf16 v[86:89], v[170:173], v[202:205], 0
	v_mfma_f32_16x16x32_bf16 v[82:85], v[178:181], v[202:205], 0
	v_mfma_f32_16x16x32_bf16 v[70:73], v[170:173], v[210:213], 0
	v_mfma_f32_16x16x32_bf16 v[66:69], v[178:181], v[210:213], 0
	v_mfma_f32_16x16x32_bf16 v[118:121], v[174:177], v[190:193], v[118:121]
	v_mfma_f32_16x16x32_bf16 v[114:117], v[182:185], v[190:193], v[114:117]
	v_mfma_f32_16x16x32_bf16 v[102:105], v[174:177], v[198:201], v[102:105]
	v_mfma_f32_16x16x32_bf16 v[98:101], v[182:185], v[198:201], v[98:101]
	v_mfma_f32_16x16x32_bf16 v[86:89], v[174:177], v[206:209], v[86:89]
	v_mfma_f32_16x16x32_bf16 v[82:85], v[182:185], v[206:209], v[82:85]
	v_mfma_f32_16x16x32_bf16 v[70:73], v[174:177], v[214:217], v[70:73]
	v_mfma_f32_16x16x32_bf16 v[66:69], v[182:185], v[214:217], v[66:69]
	s_setprio 0
	s_barrier
	s_add_i32 s62, s54, s46
	v_lshl_add_u64 v[150:151], s[40:41], 0, v[132:133]
	s_mov_b32 m0, s62
	ds_read_b128 v[186:189], v156 offset:16384
	ds_read_b128 v[190:193], v156 offset:17408
	ds_read_b128 v[194:197], v156 offset:18432
	ds_read_b128 v[198:201], v156 offset:19456
	ds_read_b128 v[202:205], v156 offset:20480
	ds_read_b128 v[206:209], v156 offset:21504
	ds_read_b128 v[210:213], v156 offset:22528
	ds_read_b128 v[214:217], v156 offset:23552
	global_load_lds_dwordx4 v[150:151], off
	s_add_i32 m0, s62, 0x2000
	s_add_u32 s68, s40, 0x80000
	v_lshl_add_u64 v[218:219], s[40:41], 0, v[136:137]
	s_addc_u32 s69, s41, 0
	s_add_i32 s62, s55, s46
	global_load_lds_dwordx4 v[218:219], off
	v_lshl_add_u64 v[220:221], s[68:69], 0, v[132:133]
	s_mov_b32 m0, s62
	v_lshl_add_u64 v[222:223], s[42:43], 0, v[134:135]
	global_load_lds_dwordx4 v[220:221], off
	v_lshl_add_u64 v[220:221], s[68:69], 0, v[136:137]
	s_add_i32 m0, s62, 0x2000
	s_nop 0
	global_load_lds_dwordx4 v[220:221], off
	v_lshl_add_u64 v[220:221], s[42:43], 0, v[130:131]
	s_mov_b32 m0, s35
	s_nop 0
	global_load_lds_dwordx4 v[220:221], off
	s_mov_b32 m0, s47
	s_nop 0
	global_load_lds_dwordx4 v[222:223], off
	s_waitcnt vmcnt(8)
	s_waitcnt lgkmcnt(0)
	s_barrier
; #define PG8_STAGE2(bufoff, gbase, v0, v1) do { \
;         __builtin_amdgcn_global_load_lds((const unsigned*)((const char*)(gbase) + (v0)), (LAS unsigned*)(lds + (bufoff) + ldsw), 16, 0, 0); \
;         __builtin_amdgcn_global_load_lds((const unsigned*)((const char*)(gbase) + (v1)), (LAS unsigned*)(lds + (bufoff) + ldsw + 8192), 16, 0, 0); } while (0)
; #define PG8_LDA(dst, b, h) do { _Pragma("unroll") for (int m = 0; m < 4; ++m) _Pragma("unroll") for (int k = 0; k < 2; ++k) dst[m][k] = *(const LAS bf16x8*)(lds + PG8_SA(b, h) + aoff + m * 2048 + k * 1024); } while (0)
; #define PG8_LDB(dst, b, h) do { _Pragma("unroll") for (int n = 0; n < 2; ++n) _Pragma("unroll") for (int k = 0; k < 2; ++k) dst[n][k] = *(const LAS bf16x8*)(lds + PG8_SB(b, h) + boff + n * 2048 + k * 1024); } while (0)
; #define PG8_MMA(ai, bj, At, Bt) do { __builtin_amdgcn_s_setprio(1); _Pragma("unroll") for (int m = 0; m < 4; ++m) _Pragma("unroll") for (int n = 0; n < 2; ++n) _Pragma("unroll") for (int k = 0; k < 2; ++k) \
;         acc[ai][bj][m][n] = __builtin_amdgcn_mfma_f32_16x16x32_bf16(Bt[n][k], At[m][k], acc[ai][bj][m][n], 0, 0, 0); __builtin_amdgcn_s_setprio(0); } while (0)
; #define PG8_WAIT_V(n) asm volatile("s_waitcnt vmcnt(" #n ")" ::: "memory")
; #define PG8_WAIT_L(n) asm volatile("s_waitcnt lgkmcnt(" #n ")" ::: "memory")
; #define PG8_BAR __builtin_amdgcn_s_barrier()
; #define PG8_SCHED __builtin_amdgcn_sched_barrier(0)
; template <class Epi, class Sched, bool ALIGN_EPI, bool SP2, bool GATHER>
; DI void gemm_phase(LAS unsigned char* lds, const Gemm g, const Sched& S, const Epi& E) {
;     ...
;             PG8_WAIT_V(8); PG8_WAIT_L(0); PG8_BAR; PG8_MMA(1, 0, At, B0); PG8_MMA(1, 1, At, B1); PG8_BAR; PG8_SCHED;
;             PG8_LDB(B0, 1, 0); PG8_LDB(B1, 1, 1); PG8_SCHED; PG8_LDA(At, 1, 0); PG8_STAGE2(PG8_SA(0, 1), a2 + hstepA, x10, x11);
;             PG8_WAIT_V(8); PG8_WAIT_L(0); PG8_BAR; PG8_MMA(0, 0, At, B0); PG8_MMA(0, 1, At, B1); PG8_BAR; PG8_SCHED;
	s_setprio 1
	s_waitcnt lgkmcnt(0)
	v_mfma_f32_16x16x32_bf16 v[62:65], v[146:149], v[186:189], 0
	v_mfma_f32_16x16x32_bf16 v[58:61], v[162:165], v[186:189], 0
	v_mfma_f32_16x16x32_bf16 v[46:49], v[146:149], v[194:197], 0
	v_mfma_f32_16x16x32_bf16 v[42:45], v[162:165], v[194:197], 0
	v_mfma_f32_16x16x32_bf16 v[22:25], v[146:149], v[202:205], 0
	v_mfma_f32_16x16x32_bf16 v[18:21], v[162:165], v[202:205], 0
	v_mfma_f32_16x16x32_bf16 v[6:9], v[146:149], v[210:213], 0
	v_mfma_f32_16x16x32_bf16 v[2:5], v[162:165], v[210:213], 0
	v_mfma_f32_16x16x32_bf16 v[62:65], v[158:161], v[190:193], v[62:65]
	v_mfma_f32_16x16x32_bf16 v[58:61], v[166:169], v[190:193], v[58:61]
	v_mfma_f32_16x16x32_bf16 v[46:49], v[158:161], v[198:201], v[46:49]
	v_mfma_f32_16x16x32_bf16 v[42:45], v[166:169], v[198:201], v[42:45]
	v_mfma_f32_16x16x32_bf16 v[22:25], v[158:161], v[206:209], v[22:25]
	v_mfma_f32_16x16x32_bf16 v[18:21], v[166:169], v[206:209], v[18:21]
	v_mfma_f32_16x16x32_bf16 v[6:9], v[158:161], v[214:217], v[6:9]
	v_mfma_f32_16x16x32_bf16 v[2:5], v[166:169], v[214:217], v[2:5]
	s_setprio 0
	s_setprio 1
	v_mfma_f32_16x16x32_bf16 v[54:57], v[170:173], v[186:189], 0
	v_mfma_f32_16x16x32_bf16 v[50:53], v[178:181], v[186:189], 0
	v_mfma_f32_16x16x32_bf16 v[30:33], v[170:173], v[194:197], 0
	v_mfma_f32_16x16x32_bf16 v[26:29], v[178:181], v[194:197], 0
	v_mfma_f32_16x16x32_bf16 v[34:37], v[170:173], v[202:205], 0
	v_mfma_f32_16x16x32_bf16 v[38:41], v[178:181], v[202:205], 0
	v_mfma_f32_16x16x32_bf16 v[10:13], v[170:173], v[210:213], 0
	v_mfma_f32_16x16x32_bf16 v[14:17], v[178:181], v[210:213], 0
	v_mfma_f32_16x16x32_bf16 v[54:57], v[174:177], v[190:193], v[54:57]
	v_mfma_f32_16x16x32_bf16 v[50:53], v[182:185], v[190:193], v[50:53]
	v_mfma_f32_16x16x32_bf16 v[30:33], v[174:177], v[198:201], v[30:33]
	v_mfma_f32_16x16x32_bf16 v[26:29], v[182:185], v[198:201], v[26:29]
	v_mfma_f32_16x16x32_bf16 v[34:37], v[174:177], v[206:209], v[34:37]
	v_mfma_f32_16x16x32_bf16 v[38:41], v[182:185], v[206:209], v[38:41]
	v_mfma_f32_16x16x32_bf16 v[10:13], v[174:177], v[214:217], v[10:13]
	v_mfma_f32_16x16x32_bf16 v[14:17], v[182:185], v[214:217], v[14:17]
	s_setprio 0
	s_barrier
	s_add_i32 s62, 0, 0x18000
	v_add_u32_e32 v157, s62, v152
	s_add_i32 s67, 0, 0x1c000
	ds_read_b128 v[146:149], v157
	ds_read_b128 v[158:161], v157 offset:1024
	ds_read_b128 v[162:165], v157 offset:2048
	ds_read_b128 v[166:169], v157 offset:3072
	v_add_u32_e32 v157, s67, v152
	ds_read_b128 v[170:173], v157
	ds_read_b128 v[174:177], v157 offset:1024
	ds_read_b128 v[178:181], v157 offset:2048
	ds_read_b128 v[182:185], v157 offset:3072
	s_add_u32 s42, s42, 0x80000
	s_addc_u32 s43, s43, 0
	s_mov_b32 m0, s48
	v_lshl_add_u64 v[224:225], s[42:43], 0, v[130:131]
	ds_read_b128 v[186:189], v156 offset:32768
	ds_read_b128 v[190:193], v156 offset:33792
	ds_read_b128 v[194:197], v156 offset:34816
	ds_read_b128 v[198:201], v156 offset:35840
	ds_read_b128 v[202:205], v156 offset:36864
	ds_read_b128 v[206:209], v156 offset:37888
	ds_read_b128 v[210:213], v156 offset:38912
	ds_read_b128 v[214:217], v156 offset:39936
	global_load_lds_dwordx4 v[224:225], off
	v_lshl_add_u64 v[224:225], s[42:43], 0, v[134:135]
	s_mov_b32 m0, s49
	s_nop 0
	global_load_lds_dwordx4 v[224:225], off
	s_waitcnt vmcnt(8)
	s_waitcnt lgkmcnt(0)
	s_barrier
	s_setprio 1
	s_waitcnt lgkmcnt(0)
	v_mfma_f32_16x16x32_bf16 v[126:129], v[146:149], v[186:189], v[126:129]
	v_mfma_f32_16x16x32_bf16 v[122:125], v[162:165], v[186:189], v[122:125]
	v_mfma_f32_16x16x32_bf16 v[110:113], v[146:149], v[194:197], v[110:113]
	v_mfma_f32_16x16x32_bf16 v[106:109], v[162:165], v[194:197], v[106:109]
	v_mfma_f32_16x16x32_bf16 v[94:97], v[146:149], v[202:205], v[94:97]
	v_mfma_f32_16x16x32_bf16 v[90:93], v[162:165], v[202:205], v[90:93]
	v_mfma_f32_16x16x32_bf16 v[78:81], v[146:149], v[210:213], v[78:81]
	v_mfma_f32_16x16x32_bf16 v[74:77], v[162:165], v[210:213], v[74:77]
	v_mfma_f32_16x16x32_bf16 v[126:129], v[158:161], v[190:193], v[126:129]
	v_mfma_f32_16x16x32_bf16 v[122:125], v[166:169], v[190:193], v[122:125]
	v_mfma_f32_16x16x32_bf16 v[110:113], v[158:161], v[198:201], v[110:113]
	v_mfma_f32_16x16x32_bf16 v[106:109], v[166:169], v[198:201], v[106:109]
	v_mfma_f32_16x16x32_bf16 v[94:97], v[158:161], v[206:209], v[94:97]
	v_mfma_f32_16x16x32_bf16 v[90:93], v[166:169], v[206:209], v[90:93]
	v_mfma_f32_16x16x32_bf16 v[78:81], v[158:161], v[214:217], v[78:81]
	v_mfma_f32_16x16x32_bf16 v[74:77], v[166:169], v[214:217], v[74:77]
	s_setprio 0
	s_setprio 1
	v_mfma_f32_16x16x32_bf16 v[118:121], v[170:173], v[186:189], v[118:121]
	v_mfma_f32_16x16x32_bf16 v[114:117], v[178:181], v[186:189], v[114:117]
	v_mfma_f32_16x16x32_bf16 v[102:105], v[170:173], v[194:197], v[102:105]
	v_mfma_f32_16x16x32_bf16 v[98:101], v[178:181], v[194:197], v[98:101]
	v_mfma_f32_16x16x32_bf16 v[86:89], v[170:173], v[202:205], v[86:89]
	v_mfma_f32_16x16x32_bf16 v[82:85], v[178:181], v[202:205], v[82:85]
	v_mfma_f32_16x16x32_bf16 v[70:73], v[170:173], v[210:213], v[70:73]
	v_mfma_f32_16x16x32_bf16 v[66:69], v[178:181], v[210:213], v[66:69]
	v_mfma_f32_16x16x32_bf16 v[118:121], v[174:177], v[190:193], v[118:121]
	v_mfma_f32_16x16x32_bf16 v[114:117], v[182:185], v[190:193], v[114:117]
	v_mfma_f32_16x16x32_bf16 v[102:105], v[174:177], v[198:201], v[102:105]
	v_mfma_f32_16x16x32_bf16 v[98:101], v[182:185], v[198:201], v[98:101]
	v_mfma_f32_16x16x32_bf16 v[86:89], v[174:177], v[206:209], v[86:89]
	v_mfma_f32_16x16x32_bf16 v[82:85], v[182:185], v[206:209], v[82:85]
	v_mfma_f32_16x16x32_bf16 v[70:73], v[174:177], v[214:217], v[70:73]
	v_mfma_f32_16x16x32_bf16 v[66:69], v[182:185], v[214:217], v[66:69]
	s_setprio 0
	s_barrier
; #define PG8_STAGE2(bufoff, gbase, v0, v1) do { \
;         __builtin_amdgcn_global_load_lds((const unsigned*)((const char*)(gbase) + (v0)), (LAS unsigned*)(lds + (bufoff) + ldsw), 16, 0, 0); \
;         __builtin_amdgcn_global_load_lds((const unsigned*)((const char*)(gbase) + (v1)), (LAS unsigned*)(lds + (bufoff) + ldsw + 8192), 16, 0, 0); } while (0)
; #define PG8_STAGE(bufoff, gbase, voff) PG8_STAGE2(bufoff, gbase, (voff)[0], (voff)[1])
; #define PG8_LDA(dst, b, h) do { _Pragma("unroll") for (int m = 0; m < 4; ++m) _Pragma("unroll") for (int k = 0; k < 2; ++k) dst[m][k] = *(const LAS bf16x8*)(lds + PG8_SA(b, h) + aoff + m * 2048 + k * 1024); } while (0)
; #define PG8_MMA(ai, bj, At, Bt) do { __builtin_amdgcn_s_setprio(1); _Pragma("unroll") for (int m = 0; m < 4; ++m) _Pragma("unroll") for (int n = 0; n < 2; ++n) _Pragma("unroll") for (int k = 0; k < 2; ++k) \
;         acc[ai][bj][m][n] = __builtin_amdgcn_mfma_f32_16x16x32_bf16(Bt[n][k], At[m][k], acc[ai][bj][m][n], 0, 0, 0); __builtin_amdgcn_s_setprio(0); } while (0)
; #define PG8_WAIT_V(n) asm volatile("s_waitcnt vmcnt(" #n ")" ::: "memory")
; #define PG8_WAIT_L(n) asm volatile("s_waitcnt lgkmcnt(" #n ")" ::: "memory")
; #define PG8_BAR __builtin_amdgcn_s_barrier()
; #define PG8_SCHED __builtin_amdgcn_sched_barrier(0)
; template <class Epi, class Sched, bool ALIGN_EPI, bool SP2, bool GATHER>
; DI void gemm_phase(LAS unsigned char* lds, const Gemm g, const Sched& S, const Epi& E) {
;     ...
;         for (int t = 0; t < nt; t += 2) {
;     ...
;             PG8_LDA(At, 1, 1); PG8_STAGE(PG8_SB(1, 0), b3, voffB); PG8_STAGE(PG8_SB(1, 1), b3 + hstep, voffB); PG8_STAGE2(PG8_SA(1, 0), a3, x00, x01);
;             PG8_WAIT_V(8); PG8_WAIT_L(0); PG8_BAR; PG8_MMA(1, 0, At, B0); PG8_MMA(1, 1, At, B1); PG8_BAR; PG8_SCHED;
	s_add_i32 s42, s62, s46
	v_lshl_add_u64 v[150:151], v[150:151], 0, s[12:13]
	s_mov_b32 m0, s42
	ds_read_b128 v[186:189], v156 offset:49152
	ds_read_b128 v[190:193], v156 offset:50176
	ds_read_b128 v[194:197], v156 offset:51200
	ds_read_b128 v[198:201], v156 offset:52224
	ds_read_b128 v[202:205], v156 offset:53248
	ds_read_b128 v[206:209], v156 offset:54272
	ds_read_b128 v[210:213], v156 offset:55296
	ds_read_b128 v[214:217], v156 offset:56320
	global_load_lds_dwordx4 v[150:151], off
	s_add_i32 m0, s42, 0x2000
	s_add_u32 s40, s40, 0x80080
	v_lshl_add_u64 v[150:151], v[218:219], 0, s[12:13]
	s_addc_u32 s41, s41, 0
	s_add_i32 s42, s67, s46
	global_load_lds_dwordx4 v[150:151], off
	v_lshl_add_u64 v[150:151], s[40:41], 0, v[132:133]
	s_mov_b32 m0, s42
	s_nop 0
	global_load_lds_dwordx4 v[150:151], off
	v_lshl_add_u64 v[150:151], s[40:41], 0, v[136:137]
	s_add_i32 m0, s42, 0x2000
	s_nop 0
	global_load_lds_dwordx4 v[150:151], off
	v_lshl_add_u64 v[150:151], v[220:221], 0, s[12:13]
	s_mov_b32 m0, s51
	s_nop 0
	global_load_lds_dwordx4 v[150:151], off
	v_lshl_add_u64 v[150:151], v[222:223], 0, s[12:13]
	s_mov_b32 m0, s52
	s_nop 0
	global_load_lds_dwordx4 v[150:151], off
	s_waitcnt vmcnt(8)
	s_waitcnt lgkmcnt(0)
	s_barrier
	s_setprio 1
	s_waitcnt lgkmcnt(0)
	v_mfma_f32_16x16x32_bf16 v[62:65], v[146:149], v[186:189], v[62:65]
	v_mfma_f32_16x16x32_bf16 v[58:61], v[162:165], v[186:189], v[58:61]
	v_mfma_f32_16x16x32_bf16 v[46:49], v[146:149], v[194:197], v[46:49]
	v_mfma_f32_16x16x32_bf16 v[42:45], v[162:165], v[194:197], v[42:45]
	v_mfma_f32_16x16x32_bf16 v[22:25], v[146:149], v[202:205], v[22:25]
	v_mfma_f32_16x16x32_bf16 v[18:21], v[162:165], v[202:205], v[18:21]
	v_mfma_f32_16x16x32_bf16 v[6:9], v[146:149], v[210:213], v[6:9]
	v_mfma_f32_16x16x32_bf16 v[2:5], v[162:165], v[210:213], v[2:5]
	v_mfma_f32_16x16x32_bf16 v[62:65], v[158:161], v[190:193], v[62:65]
	v_mfma_f32_16x16x32_bf16 v[58:61], v[166:169], v[190:193], v[58:61]
	v_mfma_f32_16x16x32_bf16 v[46:49], v[158:161], v[198:201], v[46:49]
	v_mfma_f32_16x16x32_bf16 v[42:45], v[166:169], v[198:201], v[42:45]
	v_mfma_f32_16x16x32_bf16 v[22:25], v[158:161], v[206:209], v[22:25]
	v_mfma_f32_16x16x32_bf16 v[18:21], v[166:169], v[206:209], v[18:21]
	v_mfma_f32_16x16x32_bf16 v[6:9], v[158:161], v[214:217], v[6:9]
	v_mfma_f32_16x16x32_bf16 v[2:5], v[166:169], v[214:217], v[2:5]
	s_setprio 0
	s_setprio 1
	v_mfma_f32_16x16x32_bf16 v[54:57], v[170:173], v[186:189], v[54:57]
	v_mfma_f32_16x16x32_bf16 v[50:53], v[178:181], v[186:189], v[50:53]
	v_mfma_f32_16x16x32_bf16 v[30:33], v[170:173], v[194:197], v[30:33]
	v_mfma_f32_16x16x32_bf16 v[26:29], v[178:181], v[194:197], v[26:29]
	v_mfma_f32_16x16x32_bf16 v[34:37], v[170:173], v[202:205], v[34:37]
	v_mfma_f32_16x16x32_bf16 v[38:41], v[178:181], v[202:205], v[38:41]
	v_mfma_f32_16x16x32_bf16 v[10:13], v[170:173], v[210:213], v[10:13]
	v_mfma_f32_16x16x32_bf16 v[14:17], v[178:181], v[210:213], v[14:17]
	v_mfma_f32_16x16x32_bf16 v[54:57], v[174:177], v[190:193], v[54:57]
	v_mfma_f32_16x16x32_bf16 v[50:53], v[182:185], v[190:193], v[50:53]
	v_mfma_f32_16x16x32_bf16 v[30:33], v[174:177], v[198:201], v[30:33]
	v_mfma_f32_16x16x32_bf16 v[26:29], v[182:185], v[198:201], v[26:29]
	v_mfma_f32_16x16x32_bf16 v[34:37], v[174:177], v[206:209], v[34:37]
	v_mfma_f32_16x16x32_bf16 v[38:41], v[182:185], v[206:209], v[38:41]
	v_mfma_f32_16x16x32_bf16 v[10:13], v[174:177], v[214:217], v[10:13]
	v_mfma_f32_16x16x32_bf16 v[14:17], v[182:185], v[214:217], v[14:17]
	s_setprio 0
	s_barrier
	s_add_i32 s66, s66, 2
	s_add_u32 s36, s36, 0x100
	s_addc_u32 s37, s37, 0
	s_add_u32 s64, s64, 0x100
	s_addc_u32 s65, s65, 0
	s_cmp_gt_u32 s66, 29
	s_cbranch_scc1 .Lpeel_exit_p6

; #define PG8_BAR __builtin_amdgcn_s_barrier()
; template <class Epi, class Sched, bool ALIGN_EPI, bool SP2, bool GATHER>
; DI void gemm_phase(LAS unsigned char* lds, const Gemm g, const Sched& S, const Epi& E) {
;     ...
;         if constexpr (ALIGN_EPI) { if (wr == 0) PG8_BAR; }
.Lpeel_exit_p6:
	s_and_b64 vcc, exec, s[14:15]
	s_cbranch_vccz .LBB0_677
	s_barrier

; #define PG8_STAGE2(bufoff, gbase, v0, v1) do { \
;         __builtin_amdgcn_global_load_lds((const unsigned*)((const char*)(gbase) + (v0)), (LAS unsigned*)(lds + (bufoff) + ldsw), 16, 0, 0); \
;         __builtin_amdgcn_global_load_lds((const unsigned*)((const char*)(gbase) + (v1)), (LAS unsigned*)(lds + (bufoff) + ldsw + 8192), 16, 0, 0); } while (0)
; #define PG8_STAGE(bufoff, gbase, voff) PG8_STAGE2(bufoff, gbase, (voff)[0], (voff)[1])
; #define PG8_LDA(dst, b, h) do { _Pragma("unroll") for (int m = 0; m < 4; ++m) _Pragma("unroll") for (int k = 0; k < 2; ++k) dst[m][k] = *(const LAS bf16x8*)(lds + PG8_SA(b, h) + aoff + m * 2048 + k * 1024); } while (0)
; #define PG8_WAIT_V(n) asm volatile("s_waitcnt vmcnt(" #n ")" ::: "memory")
; template <class Epi, class Sched, bool ALIGN_EPI, bool SP2, bool GATHER>
; DI void gemm_phase(LAS unsigned char* lds, const Gemm g, const Sched& S, const Epi& E) {
;     ...
;             const bool last = (t == nt - 2);
;             const char* a1 = cA + (size_t)(t + 1) * kstep;
;             const char* a2 = last ? nA : cA + (size_t)(t + 2) * kstep; const char* b2 = last ? nB : cB + (size_t)(t + 2) * kstep;
;             const char* a3 = a2 + kstep; const char* b3 = b2 + kstep;
;             unsigned x00 = gC[0][0], x01 = gC[0][1], x10 = gC[1][0], x11 = gC[1][1];
;             if constexpr (GATHER) { if (last) { x00 = gN[0][0]; x01 = gN[0][1]; x10 = gN[1][0]; x11 = gN[1][1]; } }
;             PG8_LDB(B0, 0, 0); PG8_LDB(B1, 0, 1); PG8_SCHED; PG8_LDA(At, 0, 0); PG8_STAGE2(PG8_SA(1, 1), a1 + hstepA, gC[1][0], gC[1][1]);
;             PG8_WAIT_V(8); PG8_WAIT_L(0); PG8_BAR; PG8_MMA(0, 0, At, B0); PG8_MMA(0, 1, At, B1); PG8_BAR; PG8_SCHED;
;             PG8_LDA(At, 0, 1); PG8_STAGE(PG8_SB(0, 0), b2, voffB); PG8_STAGE(PG8_SB(0, 1), b2 + hstep, voffB); PG8_STAGE2(PG8_SA(0, 0), a2, x00, x01);
;             PG8_WAIT_V(8); PG8_WAIT_L(0); PG8_BAR; PG8_MMA(1, 0, At, B0); PG8_MMA(1, 1, At, B1); PG8_BAR; PG8_SCHED;
;             PG8_LDB(B0, 1, 0); PG8_LDB(B1, 1, 1); PG8_SCHED; PG8_LDA(At, 1, 0); PG8_STAGE2(PG8_SA(0, 1), a2 + hstepA, x10, x11);
;             PG8_WAIT_V(8); PG8_WAIT_L(0); PG8_BAR; PG8_MMA(0, 0, At, B0); PG8_MMA(0, 1, At, B1); PG8_BAR; PG8_SCHED;
;     ...
;                 for (int m = 0; m < 4; ++m)
; #pragma unroll
;                     for (int n = 0; n < 2; ++n) acc[a][b][m][n] = (f32x4){0.f, 0.f, 0.f, 0.f};
.LBB0_995:
	s_ashr_i32 s15, s14, 31
	s_lshl_b64 s[20:21], s[14:15], 18
	s_add_u32 s20, s37, s20
	s_addc_u32 s21, s38, s21
	s_and_b64 s[22:23], s[18:19], exec
	s_cselect_b32 s15, s21, s29
	s_cselect_b32 s25, s20, s28
	s_ashr_i32 s17, s16, 31
	s_lshl_b64 s[22:23], s[16:17], 18
	s_add_u32 s22, s39, s22
	s_addc_u32 s23, s40, s23
	s_and_b64 s[34:35], s[18:19], exec
	s_cselect_b32 s17, s23, s31
	s_cselect_b32 s50, s22, s30
	s_add_u32 s28, s28, 0x20080
	s_addc_u32 s29, s29, 0
	s_add_u32 s51, s30, 0x100
	s_addc_u32 s52, s31, 0
	s_mov_b32 s53, -2
	ds_read_b128 v[144:147], v154
	ds_read_b128 v[148:151], v154 offset:1024
	ds_read_b128 v[158:161], v154 offset:2048
	ds_read_b128 v[162:165], v154 offset:3072
	ds_read_b128 v[166:169], v155
	ds_read_b128 v[170:173], v155 offset:1024
	ds_read_b128 v[174:177], v155 offset:2048
	ds_read_b128 v[178:181], v155 offset:3072
	s_add_u32 s30, s28, 0xfffe0080
	s_addc_u32 s31, s29, -1
	s_cmp_eq_u32 s53, 4
	s_cselect_b32 s35, s15, s31
	s_cselect_b32 s34, s25, s30
	s_cselect_b32 s31, s17, s52
	s_cselect_b32 s30, s50, s51
	v_lshl_add_u64 v[214:215], s[28:29], 0, v[140:141]
	s_add_i32 m0, s27, 0xc000
	ds_read_b128 v[182:185], v156
	ds_read_b128 v[186:189], v156 offset:1024
	ds_read_b128 v[190:193], v156 offset:2048
	ds_read_b128 v[194:197], v156 offset:3072
	ds_read_b128 v[198:201], v156 offset:4096
	ds_read_b128 v[202:205], v156 offset:5120
	ds_read_b128 v[206:209], v156 offset:6144
	ds_read_b128 v[210:213], v156 offset:7168
	global_load_lds_dwordx4 v[214:215], off
	v_lshl_add_u64 v[214:215], s[28:29], 0, v[142:143]
	s_add_i32 m0, s27, 0xe000
	s_nop 0
	global_load_lds_dwordx4 v[214:215], off
	s_waitcnt vmcnt(8)
	s_waitcnt lgkmcnt(0)
	s_barrier
	s_setprio 1
	s_waitcnt lgkmcnt(0)
	v_mfma_f32_16x16x32_bf16 v[126:129], v[144:147], v[182:185], 0
	v_mfma_f32_16x16x32_bf16 v[122:125], v[158:161], v[182:185], 0
	v_mfma_f32_16x16x32_bf16 v[110:113], v[144:147], v[190:193], 0
	v_mfma_f32_16x16x32_bf16 v[106:109], v[158:161], v[190:193], 0
	v_mfma_f32_16x16x32_bf16 v[94:97], v[144:147], v[198:201], 0
	v_mfma_f32_16x16x32_bf16 v[90:93], v[158:161], v[198:201], 0
	v_mfma_f32_16x16x32_bf16 v[78:81], v[144:147], v[206:209], 0
	v_mfma_f32_16x16x32_bf16 v[74:77], v[158:161], v[206:209], 0
	v_mfma_f32_16x16x32_bf16 v[126:129], v[148:151], v[186:189], v[126:129]
	v_mfma_f32_16x16x32_bf16 v[122:125], v[162:165], v[186:189], v[122:125]
	v_mfma_f32_16x16x32_bf16 v[110:113], v[148:151], v[194:197], v[110:113]
	v_mfma_f32_16x16x32_bf16 v[106:109], v[162:165], v[194:197], v[106:109]
	v_mfma_f32_16x16x32_bf16 v[94:97], v[148:151], v[202:205], v[94:97]
	v_mfma_f32_16x16x32_bf16 v[90:93], v[162:165], v[202:205], v[90:93]
	v_mfma_f32_16x16x32_bf16 v[78:81], v[148:151], v[210:213], v[78:81]
	v_mfma_f32_16x16x32_bf16 v[74:77], v[162:165], v[210:213], v[74:77]
	s_setprio 0
	s_setprio 1
	v_mfma_f32_16x16x32_bf16 v[118:121], v[166:169], v[182:185], 0
	v_mfma_f32_16x16x32_bf16 v[114:117], v[174:177], v[182:185], 0
	v_mfma_f32_16x16x32_bf16 v[102:105], v[166:169], v[190:193], 0
	v_mfma_f32_16x16x32_bf16 v[98:101], v[174:177], v[190:193], 0
	v_mfma_f32_16x16x32_bf16 v[86:89], v[166:169], v[198:201], 0
	v_mfma_f32_16x16x32_bf16 v[82:85], v[174:177], v[198:201], 0
	v_mfma_f32_16x16x32_bf16 v[70:73], v[166:169], v[206:209], 0
	v_mfma_f32_16x16x32_bf16 v[66:69], v[174:177], v[206:209], 0
	v_mfma_f32_16x16x32_bf16 v[118:121], v[170:173], v[186:189], v[118:121]
	v_mfma_f32_16x16x32_bf16 v[114:117], v[178:181], v[186:189], v[114:117]
	v_mfma_f32_16x16x32_bf16 v[102:105], v[170:173], v[194:197], v[102:105]
	v_mfma_f32_16x16x32_bf16 v[98:101], v[178:181], v[194:197], v[98:101]
	v_mfma_f32_16x16x32_bf16 v[86:89], v[170:173], v[202:205], v[86:89]
	v_mfma_f32_16x16x32_bf16 v[82:85], v[178:181], v[202:205], v[82:85]
	v_mfma_f32_16x16x32_bf16 v[70:73], v[170:173], v[210:213], v[70:73]
	v_mfma_f32_16x16x32_bf16 v[66:69], v[178:181], v[210:213], v[66:69]
	s_setprio 0
	s_barrier
	s_add_i32 s54, s48, s41
	v_lshl_add_u64 v[214:215], s[30:31], 0, v[132:133]
	s_mov_b32 m0, s54
	ds_read_b128 v[182:185], v156 offset:16384
	ds_read_b128 v[186:189], v156 offset:17408
	ds_read_b128 v[190:193], v156 offset:18432
	ds_read_b128 v[194:197], v156 offset:19456
	ds_read_b128 v[198:201], v156 offset:20480
	ds_read_b128 v[202:205], v156 offset:21504
	ds_read_b128 v[206:209], v156 offset:22528
	ds_read_b128 v[210:213], v156 offset:23552
	global_load_lds_dwordx4 v[214:215], off
	s_add_i32 m0, s54, 0x2000
	s_add_u32 s54, s30, 0x20000
	v_lshl_add_u64 v[216:217], s[30:31], 0, v[136:137]
	s_addc_u32 s55, s31, 0
	s_add_i32 s56, s49, s41
	global_load_lds_dwordx4 v[216:217], off
	v_lshl_add_u64 v[218:219], s[54:55], 0, v[132:133]
	s_mov_b32 m0, s56
	v_lshl_add_u64 v[220:221], s[34:35], 0, v[134:135]
	global_load_lds_dwordx4 v[218:219], off
	v_lshl_add_u64 v[218:219], s[54:55], 0, v[136:137]
	s_add_i32 m0, s56, 0x2000
	s_nop 0
	global_load_lds_dwordx4 v[218:219], off
	v_lshl_add_u64 v[218:219], s[34:35], 0, v[130:131]
	s_mov_b32 m0, s27
	s_nop 0
	global_load_lds_dwordx4 v[218:219], off
	s_mov_b32 m0, s42
	s_nop 0
	global_load_lds_dwordx4 v[220:221], off
	s_waitcnt vmcnt(8)
	s_waitcnt lgkmcnt(0)
	s_barrier
; #define PG8_STAGE2(bufoff, gbase, v0, v1) do { \
;         __builtin_amdgcn_global_load_lds((const unsigned*)((const char*)(gbase) + (v0)), (LAS unsigned*)(lds + (bufoff) + ldsw), 16, 0, 0); \
;         __builtin_amdgcn_global_load_lds((const unsigned*)((const char*)(gbase) + (v1)), (LAS unsigned*)(lds + (bufoff) + ldsw + 8192), 16, 0, 0); } while (0)
; #define PG8_LDA(dst, b, h) do { _Pragma("unroll") for (int m = 0; m < 4; ++m) _Pragma("unroll") for (int k = 0; k < 2; ++k) dst[m][k] = *(const LAS bf16x8*)(lds + PG8_SA(b, h) + aoff + m * 2048 + k * 1024); } while (0)
; #define PG8_LDB(dst, b, h) do { _Pragma("unroll") for (int n = 0; n < 2; ++n) _Pragma("unroll") for (int k = 0; k < 2; ++k) dst[n][k] = *(const LAS bf16x8*)(lds + PG8_SB(b, h) + boff + n * 2048 + k * 1024); } while (0)
; #define PG8_MMA(ai, bj, At, Bt) do { __builtin_amdgcn_s_setprio(1); _Pragma("unroll") for (int m = 0; m < 4; ++m) _Pragma("unroll") for (int n = 0; n < 2; ++n) _Pragma("unroll") for (int k = 0; k < 2; ++k) \
;         acc[ai][bj][m][n] = __builtin_amdgcn_mfma_f32_16x16x32_bf16(Bt[n][k], At[m][k], acc[ai][bj][m][n], 0, 0, 0); __builtin_amdgcn_s_setprio(0); } while (0)
; #define PG8_WAIT_V(n) asm volatile("s_waitcnt vmcnt(" #n ")" ::: "memory")
; #define PG8_WAIT_L(n) asm volatile("s_waitcnt lgkmcnt(" #n ")" ::: "memory")
; #define PG8_BAR __builtin_amdgcn_s_barrier()
; #define PG8_SCHED __builtin_amdgcn_sched_barrier(0)
; template <class Epi, class Sched, bool ALIGN_EPI, bool SP2, bool GATHER>
; DI void gemm_phase(LAS unsigned char* lds, const Gemm g, const Sched& S, const Epi& E) {
;     ...
;             PG8_WAIT_V(8); PG8_WAIT_L(0); PG8_BAR; PG8_MMA(1, 0, At, B0); PG8_MMA(1, 1, At, B1); PG8_BAR; PG8_SCHED;
;             PG8_LDB(B0, 1, 0); PG8_LDB(B1, 1, 1); PG8_SCHED; PG8_LDA(At, 1, 0); PG8_STAGE2(PG8_SA(0, 1), a2 + hstepA, x10, x11);
;             PG8_WAIT_V(8); PG8_WAIT_L(0); PG8_BAR; PG8_MMA(0, 0, At, B0); PG8_MMA(0, 1, At, B1); PG8_BAR; PG8_SCHED;
	s_setprio 1
	s_waitcnt lgkmcnt(0)
	v_mfma_f32_16x16x32_bf16 v[62:65], v[144:147], v[182:185], 0
	v_mfma_f32_16x16x32_bf16 v[58:61], v[158:161], v[182:185], 0
	v_mfma_f32_16x16x32_bf16 v[46:49], v[144:147], v[190:193], 0
	v_mfma_f32_16x16x32_bf16 v[42:45], v[158:161], v[190:193], 0
	v_mfma_f32_16x16x32_bf16 v[14:17], v[144:147], v[198:201], 0
	v_mfma_f32_16x16x32_bf16 v[10:13], v[158:161], v[198:201], 0
	v_mfma_f32_16x16x32_bf16 v[6:9], v[144:147], v[206:209], 0
	v_mfma_f32_16x16x32_bf16 v[2:5], v[158:161], v[206:209], 0
	v_mfma_f32_16x16x32_bf16 v[62:65], v[148:151], v[186:189], v[62:65]
	v_mfma_f32_16x16x32_bf16 v[58:61], v[162:165], v[186:189], v[58:61]
	v_mfma_f32_16x16x32_bf16 v[46:49], v[148:151], v[194:197], v[46:49]
	v_mfma_f32_16x16x32_bf16 v[42:45], v[162:165], v[194:197], v[42:45]
	v_mfma_f32_16x16x32_bf16 v[14:17], v[148:151], v[202:205], v[14:17]
	v_mfma_f32_16x16x32_bf16 v[10:13], v[162:165], v[202:205], v[10:13]
	v_mfma_f32_16x16x32_bf16 v[6:9], v[148:151], v[210:213], v[6:9]
	v_mfma_f32_16x16x32_bf16 v[2:5], v[162:165], v[210:213], v[2:5]
	s_setprio 0
	s_setprio 1
	v_mfma_f32_16x16x32_bf16 v[54:57], v[166:169], v[182:185], 0
	v_mfma_f32_16x16x32_bf16 v[50:53], v[174:177], v[182:185], 0
	v_mfma_f32_16x16x32_bf16 v[30:33], v[166:169], v[190:193], 0
	v_mfma_f32_16x16x32_bf16 v[26:29], v[174:177], v[190:193], 0
	v_mfma_f32_16x16x32_bf16 v[34:37], v[166:169], v[198:201], 0
	v_mfma_f32_16x16x32_bf16 v[38:41], v[174:177], v[198:201], 0
	v_mfma_f32_16x16x32_bf16 v[18:21], v[166:169], v[206:209], 0
	v_mfma_f32_16x16x32_bf16 v[22:25], v[174:177], v[206:209], 0
	v_mfma_f32_16x16x32_bf16 v[54:57], v[170:173], v[186:189], v[54:57]
	v_mfma_f32_16x16x32_bf16 v[50:53], v[178:181], v[186:189], v[50:53]
	v_mfma_f32_16x16x32_bf16 v[30:33], v[170:173], v[194:197], v[30:33]
	v_mfma_f32_16x16x32_bf16 v[26:29], v[178:181], v[194:197], v[26:29]
	v_mfma_f32_16x16x32_bf16 v[34:37], v[170:173], v[202:205], v[34:37]
	v_mfma_f32_16x16x32_bf16 v[38:41], v[178:181], v[202:205], v[38:41]
	v_mfma_f32_16x16x32_bf16 v[18:21], v[170:173], v[210:213], v[18:21]
	v_mfma_f32_16x16x32_bf16 v[22:25], v[178:181], v[210:213], v[22:25]
	s_setprio 0
	s_barrier
	s_add_i32 s54, 0, 0x18000
	v_add_u32_e32 v138, s54, v152
	s_add_i32 s55, 0, 0x1c000
	ds_read_b128 v[144:147], v138
	ds_read_b128 v[148:151], v138 offset:1024
	ds_read_b128 v[158:161], v138 offset:2048
	ds_read_b128 v[162:165], v138 offset:3072
	v_add_u32_e32 v138, s55, v152
	ds_read_b128 v[166:169], v138
	ds_read_b128 v[170:173], v138 offset:1024
	ds_read_b128 v[174:177], v138 offset:2048
	ds_read_b128 v[178:181], v138 offset:3072
	s_add_u32 s34, s34, 0x20000
	s_addc_u32 s35, s35, 0
	s_mov_b32 m0, s43
	v_lshl_add_u64 v[222:223], s[34:35], 0, v[130:131]
	ds_read_b128 v[182:185], v156 offset:32768
	ds_read_b128 v[186:189], v156 offset:33792
	ds_read_b128 v[190:193], v156 offset:34816
	ds_read_b128 v[194:197], v156 offset:35840
	ds_read_b128 v[198:201], v156 offset:36864
	ds_read_b128 v[202:205], v156 offset:37888
	ds_read_b128 v[206:209], v156 offset:38912
	ds_read_b128 v[210:213], v156 offset:39936
	global_load_lds_dwordx4 v[222:223], off
	v_lshl_add_u64 v[222:223], s[34:35], 0, v[134:135]
	s_mov_b32 m0, s44
	s_nop 0
	global_load_lds_dwordx4 v[222:223], off
	s_waitcnt vmcnt(8)
	s_waitcnt lgkmcnt(0)
	s_barrier
	s_setprio 1
	s_waitcnt lgkmcnt(0)
	v_mfma_f32_16x16x32_bf16 v[126:129], v[144:147], v[182:185], v[126:129]
	v_mfma_f32_16x16x32_bf16 v[122:125], v[158:161], v[182:185], v[122:125]
	v_mfma_f32_16x16x32_bf16 v[110:113], v[144:147], v[190:193], v[110:113]
	v_mfma_f32_16x16x32_bf16 v[106:109], v[158:161], v[190:193], v[106:109]
	v_mfma_f32_16x16x32_bf16 v[94:97], v[144:147], v[198:201], v[94:97]
	v_mfma_f32_16x16x32_bf16 v[90:93], v[158:161], v[198:201], v[90:93]
	v_mfma_f32_16x16x32_bf16 v[78:81], v[144:147], v[206:209], v[78:81]
	v_mfma_f32_16x16x32_bf16 v[74:77], v[158:161], v[206:209], v[74:77]
	v_mfma_f32_16x16x32_bf16 v[126:129], v[148:151], v[186:189], v[126:129]
	v_mfma_f32_16x16x32_bf16 v[122:125], v[162:165], v[186:189], v[122:125]
	v_mfma_f32_16x16x32_bf16 v[110:113], v[148:151], v[194:197], v[110:113]
	v_mfma_f32_16x16x32_bf16 v[106:109], v[162:165], v[194:197], v[106:109]
	v_mfma_f32_16x16x32_bf16 v[94:97], v[148:151], v[202:205], v[94:97]
	v_mfma_f32_16x16x32_bf16 v[90:93], v[162:165], v[202:205], v[90:93]
	v_mfma_f32_16x16x32_bf16 v[78:81], v[148:151], v[210:213], v[78:81]
	v_mfma_f32_16x16x32_bf16 v[74:77], v[162:165], v[210:213], v[74:77]
	s_setprio 0
	s_setprio 1
	v_mfma_f32_16x16x32_bf16 v[118:121], v[166:169], v[182:185], v[118:121]
	v_mfma_f32_16x16x32_bf16 v[114:117], v[174:177], v[182:185], v[114:117]
	v_mfma_f32_16x16x32_bf16 v[102:105], v[166:169], v[190:193], v[102:105]
	v_mfma_f32_16x16x32_bf16 v[98:101], v[174:177], v[190:193], v[98:101]
	v_mfma_f32_16x16x32_bf16 v[86:89], v[166:169], v[198:201], v[86:89]
	v_mfma_f32_16x16x32_bf16 v[82:85], v[174:177], v[198:201], v[82:85]
	v_mfma_f32_16x16x32_bf16 v[70:73], v[166:169], v[206:209], v[70:73]
	v_mfma_f32_16x16x32_bf16 v[66:69], v[174:177], v[206:209], v[66:69]
	v_mfma_f32_16x16x32_bf16 v[118:121], v[170:173], v[186:189], v[118:121]
	v_mfma_f32_16x16x32_bf16 v[114:117], v[178:181], v[186:189], v[114:117]
	v_mfma_f32_16x16x32_bf16 v[102:105], v[170:173], v[194:197], v[102:105]
	v_mfma_f32_16x16x32_bf16 v[98:101], v[178:181], v[194:197], v[98:101]
	v_mfma_f32_16x16x32_bf16 v[86:89], v[170:173], v[202:205], v[86:89]
	v_mfma_f32_16x16x32_bf16 v[82:85], v[178:181], v[202:205], v[82:85]
	v_mfma_f32_16x16x32_bf16 v[70:73], v[170:173], v[210:213], v[70:73]
	v_mfma_f32_16x16x32_bf16 v[66:69], v[178:181], v[210:213], v[66:69]
	s_setprio 0
	s_barrier
; #define PG8_STAGE2(bufoff, gbase, v0, v1) do { \
;         __builtin_amdgcn_global_load_lds((const unsigned*)((const char*)(gbase) + (v0)), (LAS unsigned*)(lds + (bufoff) + ldsw), 16, 0, 0); \
;         __builtin_amdgcn_global_load_lds((const unsigned*)((const char*)(gbase) + (v1)), (LAS unsigned*)(lds + (bufoff) + ldsw + 8192), 16, 0, 0); } while (0)
; #define PG8_STAGE(bufoff, gbase, voff) PG8_STAGE2(bufoff, gbase, (voff)[0], (voff)[1])
; #define PG8_LDA(dst, b, h) do { _Pragma("unroll") for (int m = 0; m < 4; ++m) _Pragma("unroll") for (int k = 0; k < 2; ++k) dst[m][k] = *(const LAS bf16x8*)(lds + PG8_SA(b, h) + aoff + m * 2048 + k * 1024); } while (0)
; #define PG8_MMA(ai, bj, At, Bt) do { __builtin_amdgcn_s_setprio(1); _Pragma("unroll") for (int m = 0; m < 4; ++m) _Pragma("unroll") for (int n = 0; n < 2; ++n) _Pragma("unroll") for (int k = 0; k < 2; ++k) \
;         acc[ai][bj][m][n] = __builtin_amdgcn_mfma_f32_16x16x32_bf16(Bt[n][k], At[m][k], acc[ai][bj][m][n], 0, 0, 0); __builtin_amdgcn_s_setprio(0); } while (0)
; #define PG8_WAIT_V(n) asm volatile("s_waitcnt vmcnt(" #n ")" ::: "memory")
; #define PG8_WAIT_L(n) asm volatile("s_waitcnt lgkmcnt(" #n ")" ::: "memory")
; #define PG8_BAR __builtin_amdgcn_s_barrier()
; #define PG8_SCHED __builtin_amdgcn_sched_barrier(0)
; template <class Epi, class Sched, bool ALIGN_EPI, bool SP2, bool GATHER>
; DI void gemm_phase(LAS unsigned char* lds, const Gemm g, const Sched& S, const Epi& E) {
;     ...
;         for (int t = 0; t < nt; t += 2) {
;     ...
;             PG8_LDA(At, 1, 1); PG8_STAGE(PG8_SB(1, 0), b3, voffB); PG8_STAGE(PG8_SB(1, 1), b3 + hstep, voffB); PG8_STAGE2(PG8_SA(1, 0), a3, x00, x01);
;             PG8_WAIT_V(8); PG8_WAIT_L(0); PG8_BAR; PG8_MMA(1, 0, At, B0); PG8_MMA(1, 1, At, B1); PG8_BAR; PG8_SCHED;
	s_add_i32 s34, s54, s41
	v_lshl_add_u64 v[214:215], v[214:215], 0, s[10:11]
	s_mov_b32 m0, s34
	ds_read_b128 v[182:185], v156 offset:49152
	ds_read_b128 v[186:189], v156 offset:50176
	ds_read_b128 v[190:193], v156 offset:51200
	ds_read_b128 v[194:197], v156 offset:52224
	ds_read_b128 v[198:201], v156 offset:53248
	ds_read_b128 v[202:205], v156 offset:54272
	ds_read_b128 v[206:209], v156 offset:55296
	ds_read_b128 v[210:213], v156 offset:56320
	global_load_lds_dwordx4 v[214:215], off
	s_add_i32 m0, s34, 0x2000
	s_add_u32 s30, s30, 0x20080
	v_lshl_add_u64 v[214:215], v[216:217], 0, s[10:11]
	s_addc_u32 s31, s31, 0
	s_add_i32 s34, s55, s41
	global_load_lds_dwordx4 v[214:215], off
	v_lshl_add_u64 v[214:215], s[30:31], 0, v[132:133]
	s_mov_b32 m0, s34
	s_nop 0
	global_load_lds_dwordx4 v[214:215], off
	v_lshl_add_u64 v[214:215], s[30:31], 0, v[136:137]
	s_add_i32 m0, s34, 0x2000
	s_nop 0
	global_load_lds_dwordx4 v[214:215], off
	v_lshl_add_u64 v[214:215], v[218:219], 0, s[10:11]
	s_mov_b32 m0, s46
	s_nop 0
	global_load_lds_dwordx4 v[214:215], off
	v_lshl_add_u64 v[214:215], v[220:221], 0, s[10:11]
	s_mov_b32 m0, s47
	s_nop 0
	global_load_lds_dwordx4 v[214:215], off
	s_waitcnt vmcnt(8)
	s_waitcnt lgkmcnt(0)
	s_barrier
	s_setprio 1
	s_waitcnt lgkmcnt(0)
	v_mfma_f32_16x16x32_bf16 v[62:65], v[144:147], v[182:185], v[62:65]
	v_mfma_f32_16x16x32_bf16 v[58:61], v[158:161], v[182:185], v[58:61]
	v_mfma_f32_16x16x32_bf16 v[46:49], v[144:147], v[190:193], v[46:49]
	v_mfma_f32_16x16x32_bf16 v[42:45], v[158:161], v[190:193], v[42:45]
	v_mfma_f32_16x16x32_bf16 v[14:17], v[144:147], v[198:201], v[14:17]
	v_mfma_f32_16x16x32_bf16 v[10:13], v[158:161], v[198:201], v[10:13]
	v_mfma_f32_16x16x32_bf16 v[6:9], v[144:147], v[206:209], v[6:9]
	v_mfma_f32_16x16x32_bf16 v[2:5], v[158:161], v[206:209], v[2:5]
	v_mfma_f32_16x16x32_bf16 v[62:65], v[148:151], v[186:189], v[62:65]
	v_mfma_f32_16x16x32_bf16 v[58:61], v[162:165], v[186:189], v[58:61]
	v_mfma_f32_16x16x32_bf16 v[46:49], v[148:151], v[194:197], v[46:49]
	v_mfma_f32_16x16x32_bf16 v[42:45], v[162:165], v[194:197], v[42:45]
	v_mfma_f32_16x16x32_bf16 v[14:17], v[148:151], v[202:205], v[14:17]
	v_mfma_f32_16x16x32_bf16 v[10:13], v[162:165], v[202:205], v[10:13]
	v_mfma_f32_16x16x32_bf16 v[6:9], v[148:151], v[210:213], v[6:9]
	v_mfma_f32_16x16x32_bf16 v[2:5], v[162:165], v[210:213], v[2:5]
	s_setprio 0
	s_setprio 1
	v_mfma_f32_16x16x32_bf16 v[54:57], v[166:169], v[182:185], v[54:57]
	v_mfma_f32_16x16x32_bf16 v[50:53], v[174:177], v[182:185], v[50:53]
	v_mfma_f32_16x16x32_bf16 v[30:33], v[166:169], v[190:193], v[30:33]
	v_mfma_f32_16x16x32_bf16 v[26:29], v[174:177], v[190:193], v[26:29]
	v_mfma_f32_16x16x32_bf16 v[34:37], v[166:169], v[198:201], v[34:37]
	v_mfma_f32_16x16x32_bf16 v[38:41], v[174:177], v[198:201], v[38:41]
	v_mfma_f32_16x16x32_bf16 v[18:21], v[166:169], v[206:209], v[18:21]
	v_mfma_f32_16x16x32_bf16 v[22:25], v[174:177], v[206:209], v[22:25]
	v_mfma_f32_16x16x32_bf16 v[54:57], v[170:173], v[186:189], v[54:57]
	v_mfma_f32_16x16x32_bf16 v[50:53], v[178:181], v[186:189], v[50:53]
	v_mfma_f32_16x16x32_bf16 v[30:33], v[170:173], v[194:197], v[30:33]
	v_mfma_f32_16x16x32_bf16 v[26:29], v[178:181], v[194:197], v[26:29]
	v_mfma_f32_16x16x32_bf16 v[34:37], v[170:173], v[202:205], v[34:37]
	v_mfma_f32_16x16x32_bf16 v[38:41], v[178:181], v[202:205], v[38:41]
	v_mfma_f32_16x16x32_bf16 v[18:21], v[170:173], v[210:213], v[18:21]
	v_mfma_f32_16x16x32_bf16 v[22:25], v[178:181], v[210:213], v[22:25]
	s_setprio 0
	s_barrier
	s_add_i32 s53, s53, 2
	s_add_u32 s28, s28, 0x100
	s_addc_u32 s29, s29, 0
	s_add_u32 s51, s51, 0x100
	s_addc_u32 s52, s52, 0
	s_cmp_gt_u32 s53, 5
	s_cbranch_scc1 .Lpeel_exit_p10

; #define PG8_BAR __builtin_amdgcn_s_barrier()
; template <class Epi, class Sched, bool ALIGN_EPI, bool SP2, bool GATHER>
; DI void gemm_phase(LAS unsigned char* lds, const Gemm g, const Sched& S, const Epi& E) {
;     ...
;         if constexpr (ALIGN_EPI) { if (wr == 0) PG8_BAR; }
.Lpeel_exit_p10:
	s_and_b64 vcc, exec, s[12:13]
	s_cbranch_vccz .LBB0_999
	s_barrier
